# v59 + code placement: the eight hot-loop heads (three attention KV loops, five GEMM K-loops) start on 64-byte boundaries (s_nop padding off the hot path)
# baseline (speedup 1.0000x reference)
.LBB0_512:
	s_and_b64 s[2:3], s[84:85], exec
	s_cselect_b32 s2, s71, s53
	s_lshr_b32 s2, s2, 12
	s_and_b32 s72, s2, 0x80000
	s_and_b64 s[2:3], s[84:85], exec
	s_cselect_b32 s67, s77, s83
	s_cselect_b32 s75, s76, s82
	s_cselect_b32 s95, s79, s23
	s_cselect_b32 s29, s78, s22
	s_cmp_lt_i32 s53, 0
	s_cselect_b64 s[96:97], -1, 0
	s_add_u32 s3, s22, 0x100
	s_addc_u32 s2, s23, 0
	s_add_u32 s22, s82, 0x80
	s_addc_u32 s23, s83, 0
	v_lshl_add_u64 v[0:1], s[22:23], 0, v[206:207]
	v_lshl_add_u64 v[210:211], v[0:1], 0, s[86:87]
	v_lshl_add_u64 v[0:1], s[22:23], 0, v[208:209]
	v_mov_b32_e32 v2, v129
	v_mov_b32_e32 v3, v129
	v_lshl_add_u64 v[212:213], v[0:1], 0, s[86:87]
	v_mov_b32_e32 v0, v129
	v_mov_b32_e32 v1, v129
	v_mov_b32_e32 v64, 0
	v_mov_b64_e32 v[6:7], v[2:3]
	v_mov_b64_e32 v[18:19], v[2:3]
	v_mov_b64_e32 v[22:23], v[2:3]
	v_mov_b64_e32 v[34:35], v[2:3]
	v_mov_b64_e32 v[38:39], v[2:3]
	v_mov_b64_e32 v[50:51], v[2:3]
	v_mov_b64_e32 v[54:55], v[2:3]
	v_mov_b64_e32 v[10:11], v[2:3]
	v_mov_b64_e32 v[14:15], v[2:3]
	v_mov_b64_e32 v[26:27], v[2:3]
	v_mov_b64_e32 v[30:31], v[2:3]
	v_mov_b64_e32 v[42:43], v[2:3]
	v_mov_b64_e32 v[46:47], v[2:3]
	v_mov_b64_e32 v[58:59], v[2:3]
	v_mov_b64_e32 v[62:63], v[2:3]
	s_mov_b32 s30, -2
	v_mov_b64_e32 v[4:5], v[0:1]
	v_mov_b64_e32 v[16:17], v[0:1]
	v_mov_b64_e32 v[20:21], v[0:1]
	v_mov_b64_e32 v[32:33], v[0:1]
	v_mov_b64_e32 v[36:37], v[0:1]
	v_mov_b64_e32 v[48:49], v[0:1]
	v_mov_b64_e32 v[52:53], v[0:1]
	v_mov_b64_e32 v[8:9], v[0:1]
	v_mov_b64_e32 v[12:13], v[0:1]
	v_mov_b64_e32 v[24:25], v[0:1]
	v_mov_b64_e32 v[28:29], v[0:1]
	v_mov_b64_e32 v[40:41], v[0:1]
	v_mov_b64_e32 v[44:45], v[0:1]
	v_mov_b64_e32 v[56:57], v[0:1]
	v_mov_b64_e32 v[60:61], v[0:1]
	v_mov_b32_e32 v65, v64
	v_mov_b32_e32 v66, v64
	v_mov_b32_e32 v67, v64
	v_mov_b32_e32 v68, v64
	v_mov_b32_e32 v69, v64
	v_mov_b32_e32 v70, v64
	v_mov_b32_e32 v71, v64
	v_mov_b32_e32 v72, v64
	v_mov_b32_e32 v73, v64
	v_mov_b32_e32 v74, v64
	v_mov_b32_e32 v75, v64
	v_mov_b32_e32 v80, v64
	v_mov_b32_e32 v81, v64
	v_mov_b32_e32 v82, v64
	v_mov_b32_e32 v83, v64
	v_mov_b32_e32 v88, v64
	v_mov_b32_e32 v89, v64
	v_mov_b32_e32 v90, v64
	v_mov_b32_e32 v91, v64
	v_mov_b32_e32 v96, v64
	v_mov_b32_e32 v97, v64
	v_mov_b32_e32 v98, v64
	v_mov_b32_e32 v99, v64
	v_mov_b32_e32 v104, v64
	v_mov_b32_e32 v105, v64
	v_mov_b32_e32 v106, v64
	v_mov_b32_e32 v107, v64
	v_mov_b32_e32 v112, v64
	v_mov_b32_e32 v113, v64
	v_mov_b32_e32 v114, v64
	v_mov_b32_e32 v115, v64
	v_mov_b32_e32 v76, v64
	v_mov_b32_e32 v77, v64
	v_mov_b32_e32 v78, v64
	v_mov_b32_e32 v79, v64
	v_mov_b32_e32 v84, v64
	v_mov_b32_e32 v85, v64
	v_mov_b32_e32 v86, v64
	v_mov_b32_e32 v87, v64
	v_mov_b32_e32 v92, v64
	v_mov_b32_e32 v93, v64
	v_mov_b32_e32 v94, v64
	v_mov_b32_e32 v95, v64
	v_mov_b32_e32 v100, v64
	v_mov_b32_e32 v101, v64
	v_mov_b32_e32 v102, v64
	v_mov_b32_e32 v103, v64
	v_mov_b32_e32 v108, v64
	v_mov_b32_e32 v109, v64
	v_mov_b32_e32 v110, v64
	v_mov_b32_e32 v111, v64
	v_mov_b32_e32 v116, v64
	v_mov_b32_e32 v117, v64
	v_mov_b32_e32 v118, v64
	v_mov_b32_e32 v119, v64
	v_mov_b32_e32 v120, v64
	v_mov_b32_e32 v121, v64
	v_mov_b32_e32 v122, v64
	v_mov_b32_e32 v123, v64
	v_mov_b32_e32 v124, v64
	v_mov_b32_e32 v125, v64
	v_mov_b32_e32 v126, v64
	v_mov_b32_e32 v127, v64
	s_branch .LBB0_514
	.p2alignl 6, 3212836864

.LBB0_724:
	s_add_u32 s64, s22, 0x20080
	s_addc_u32 s65, s23, 0
	s_add_u32 s15, s66, 0x100
	v_mov_b32_e32 v0, 0
	s_addc_u32 s17, s67, 0
	s_mov_b32 s66, -2
	v_mov_b32_e32 v1, v0
	v_mov_b32_e32 v2, v0
	v_mov_b32_e32 v3, v0
	v_mov_b32_e32 v4, v0
	v_mov_b32_e32 v5, v0
	v_mov_b32_e32 v6, v0
	v_mov_b32_e32 v7, v0
	v_mov_b32_e32 v8, v0
	v_mov_b32_e32 v9, v0
	v_mov_b32_e32 v10, v0
	v_mov_b32_e32 v11, v0
	v_mov_b32_e32 v16, v0
	v_mov_b32_e32 v17, v0
	v_mov_b32_e32 v18, v0
	v_mov_b32_e32 v19, v0
	v_mov_b32_e32 v24, v0
	v_mov_b32_e32 v25, v0
	v_mov_b32_e32 v26, v0
	v_mov_b32_e32 v27, v0
	v_mov_b32_e32 v32, v0
	v_mov_b32_e32 v33, v0
	v_mov_b32_e32 v34, v0
	v_mov_b32_e32 v35, v0
	v_mov_b32_e32 v40, v0
	v_mov_b32_e32 v41, v0
	v_mov_b32_e32 v42, v0
	v_mov_b32_e32 v43, v0
	v_mov_b32_e32 v48, v0
	v_mov_b32_e32 v49, v0
	v_mov_b32_e32 v50, v0
	v_mov_b32_e32 v51, v0
	v_mov_b32_e32 v12, v0
	v_mov_b32_e32 v13, v0
	v_mov_b32_e32 v14, v0
	v_mov_b32_e32 v15, v0
	v_mov_b32_e32 v20, v0
	v_mov_b32_e32 v21, v0
	v_mov_b32_e32 v22, v0
	v_mov_b32_e32 v23, v0
	v_mov_b32_e32 v28, v0
	v_mov_b32_e32 v29, v0
	v_mov_b32_e32 v30, v0
	v_mov_b32_e32 v31, v0
	v_mov_b32_e32 v36, v0
	v_mov_b32_e32 v37, v0
	v_mov_b32_e32 v38, v0
	v_mov_b32_e32 v39, v0
	v_mov_b32_e32 v44, v0
	v_mov_b32_e32 v45, v0
	v_mov_b32_e32 v46, v0
	v_mov_b32_e32 v47, v0
	v_mov_b32_e32 v52, v0
	v_mov_b32_e32 v53, v0
	v_mov_b32_e32 v54, v0
	v_mov_b32_e32 v55, v0
	v_mov_b32_e32 v56, v0
	v_mov_b32_e32 v57, v0
	v_mov_b32_e32 v58, v0
	v_mov_b32_e32 v59, v0
	v_mov_b32_e32 v60, v0
	v_mov_b32_e32 v61, v0
	v_mov_b32_e32 v62, v0
	v_mov_b32_e32 v63, v0
	v_mov_b32_e32 v64, v0
	v_mov_b32_e32 v65, v0
	v_mov_b32_e32 v66, v0
	v_mov_b32_e32 v67, v0
	v_mov_b32_e32 v68, v0
	v_mov_b32_e32 v69, v0
	v_mov_b32_e32 v70, v0
	v_mov_b32_e32 v71, v0
	v_mov_b32_e32 v72, v0
	v_mov_b32_e32 v73, v0
	v_mov_b32_e32 v74, v0
	v_mov_b32_e32 v75, v0
	v_mov_b32_e32 v80, v0
	v_mov_b32_e32 v81, v0
	v_mov_b32_e32 v82, v0
	v_mov_b32_e32 v83, v0
	v_mov_b32_e32 v88, v0
	v_mov_b32_e32 v89, v0
	v_mov_b32_e32 v90, v0
	v_mov_b32_e32 v91, v0
	v_mov_b32_e32 v96, v0
	v_mov_b32_e32 v97, v0
	v_mov_b32_e32 v98, v0
	v_mov_b32_e32 v99, v0
	v_mov_b32_e32 v104, v0
	v_mov_b32_e32 v105, v0
	v_mov_b32_e32 v106, v0
	v_mov_b32_e32 v107, v0
	v_mov_b32_e32 v112, v0
	v_mov_b32_e32 v113, v0
	v_mov_b32_e32 v114, v0
	v_mov_b32_e32 v115, v0
	v_mov_b32_e32 v76, v0
	v_mov_b32_e32 v77, v0
	v_mov_b32_e32 v78, v0
	v_mov_b32_e32 v79, v0
	v_mov_b32_e32 v84, v0
	v_mov_b32_e32 v85, v0
	v_mov_b32_e32 v86, v0
	v_mov_b32_e32 v87, v0
	v_mov_b32_e32 v92, v0
	v_mov_b32_e32 v93, v0
	v_mov_b32_e32 v94, v0
	v_mov_b32_e32 v95, v0
	v_mov_b32_e32 v100, v0
	v_mov_b32_e32 v101, v0
	v_mov_b32_e32 v102, v0
	v_mov_b32_e32 v103, v0
	v_mov_b32_e32 v108, v0
	v_mov_b32_e32 v109, v0
	v_mov_b32_e32 v110, v0
	v_mov_b32_e32 v111, v0
	v_mov_b32_e32 v116, v0
	v_mov_b32_e32 v117, v0
	v_mov_b32_e32 v118, v0
	v_mov_b32_e32 v119, v0
	v_mov_b32_e32 v120, v0
	v_mov_b32_e32 v121, v0
	v_mov_b32_e32 v122, v0
	v_mov_b32_e32 v123, v0
	v_mov_b32_e32 v124, v0
	v_mov_b32_e32 v125, v0
	v_mov_b32_e32 v126, v0
	v_mov_b32_e32 v127, v0
	.p2alignl 6, 3212836864

.LBB0_812:
	s_or_b64 exec, exec, s[6:7]
	s_lshl_b32 s6, s16, 8
	s_mul_i32 s8, s30, 0x900
	s_ashr_i32 s7, s6, 31
	s_mul_hi_i32 s3, s30, 0x900
	s_add_u32 s78, s8, s6
	s_addc_u32 s79, s3, s7
	s_mul_i32 s6, s78, s69
	s_mul_hi_u32 s7, s78, s68
	s_add_i32 s6, s7, s6
	s_mul_i32 s7, s79, s68
	s_add_i32 s7, s6, s7
	s_mul_i32 s6, s78, s68
	s_lshl_b64 s[6:7], s[6:7], 1
	s_add_u32 s9, s60, s6
	s_mul_i32 s6, s15, s26
	s_addc_u32 s11, s61, s7
	s_ashr_i32 s7, s6, 31
	s_lshl_b64 s[6:7], s[6:7], 1
	s_add_u32 s10, s9, s6
	s_mul_i32 s3, s3, s62
	s_mul_hi_u32 s6, s8, s62
	s_addc_u32 s11, s11, s7
	s_add_i32 s7, s6, s3
	s_mul_i32 s6, s8, s62
	s_lshl_b64 s[8:9], s[6:7], 1
	s_add_u32 s3, s66, s8
	s_addc_u32 s22, s67, s9
	s_abs_i32 s7, s15
	s_mul_hi_u32 s20, s7, s13
	s_mul_i32 s21, s20, s89
	s_sub_i32 s7, s7, s21
	s_ashr_i32 s6, s15, 31
	s_add_i32 s21, s20, 1
	s_sub_i32 s23, s7, s89
	s_cmp_ge_u32 s7, s89
	s_cselect_b32 s20, s21, s20
	v_ashrrev_i32_e32 v20, 4, v8
	v_and_b32_e32 v3, 0xfffff0, v20
	v_lshlrev_b32_e32 v4, 1, v20
	s_cselect_b32 s7, s23, s7
	s_add_i32 s21, s20, 1
	v_lshlrev_b32_e32 v1, 3, v8
	v_and_or_b32 v3, v4, 8, v3
	s_cmp_ge_u32 s7, s89
	v_and_b32_e32 v2, 0x78, v1
	v_lshrrev_b32_e32 v3, 1, v3
	v_bfe_u32 v1, v1, 5, 2
	s_cselect_b32 s7, s21, s20
	v_or_b32_e32 v3, v3, v1
	s_xor_b32 s7, s7, s6
	v_lshrrev_b32_e32 v4, 1, v20
	v_lshlrev_b32_e32 v21, 9, v3
	v_and_b32_e32 v3, 3, v20
	s_sub_i32 s6, s7, s6
	v_and_or_b32 v3, v4, 4, v3
	v_add_u32_e32 v24, 32, v20
	s_mul_i32 s6, s6, s27
	v_lshlrev_b32_e32 v22, 6, v3
	v_and_b32_e32 v3, 0xfffff0, v24
	v_lshlrev_b32_e32 v4, 1, v24
	s_ashr_i32 s7, s6, 31
	v_and_or_b32 v3, v4, 8, v3
	s_lshl_b64 s[20:21], s[6:7], 1
	v_lshrrev_b32_e32 v3, 1, v3
	s_add_u32 s6, s3, s20
	v_or_b32_e32 v1, v3, v1
	s_addc_u32 s7, s22, s21
	v_lshlrev_b32_e32 v25, 9, v1
	v_mul_lo_u32 v1, v20, s62
	s_add_u32 s3, s85, s8
	v_or_b32_e32 v3, v1, v2
	v_add_u32_e32 v1, s14, v1
	s_addc_u32 s9, s81, s9
	v_and_b32_e32 v0, 63, v8
	v_or_b32_e32 v1, v1, v2
	v_lshlrev_b32_e32 v26, 4, v8
	s_add_u32 s8, s3, s20
	v_lshlrev_b32_e32 v23, 1, v2
	v_lshlrev_b32_e32 v178, 1, v1
	v_lshlrev_b32_e32 v0, 3, v0
	v_and_b32_e32 v1, 0xc0, v26
	v_lshlrev_b32_e32 v2, 1, v8
	s_addc_u32 s9, s9, s21
	v_lshlrev_b32_e32 v128, 1, v3
	v_and_or_b32 v1, v0, 24, v1
	v_and_b32_e32 v2, 32, v2
	v_and_b32_e32 v0, 0x100, v0
	v_or3_b32 v181, v1, v2, v0
	global_load_dwordx4 v[10:13], v128, s[8:9]
	global_load_dwordx4 v[14:17], v178, s[8:9]
	global_load_dwordx4 v[4:7], v128, s[6:7]
	global_load_dwordx4 v[0:3], v178, s[6:7]
	v_ashrrev_i32_e32 v27, 1, v8
	v_bfi_b32 v18, s84, v27, v8
	v_ashrrev_i32_e32 v19, 31, v27
	v_mul_lo_u32 v28, s68, v19
	v_mul_lo_u32 v29, s69, v18
	v_mad_u64_u32 v[18:19], s[20:21], s68, v18, 0
	v_bfe_u32 v182, v8, 5, 1
	v_add3_u32 v19, v19, v28, v29
	v_lshl_add_u64 v[18:19], v[18:19], 1, s[10:11]
	v_lshlrev_b32_e32 v32, 4, v182
	v_mov_b32_e32 v33, v129
	v_lshl_add_u64 v[18:19], v[18:19], 0, v[32:33]
	global_load_dwordx4 v[120:123], v[18:19], off
	global_load_dwordx4 v[124:127], v[18:19], off offset:32
	global_load_dwordx4 v[116:119], v[18:19], off offset:64
	global_load_dwordx4 v[112:115], v[18:19], off offset:96
	global_load_dwordx4 v[108:111], v[18:19], off offset:128
	global_load_dwordx4 v[104:107], v[18:19], off offset:160
	global_load_dwordx4 v[100:103], v[18:19], off offset:192
	global_load_dwordx4 v[96:99], v[18:19], off offset:224
	v_and_b32_e32 v18, 48, v23
	v_or3_b32 v19, v21, v22, v18
	v_add_u32_e32 v201, 0, v19
	v_lshrrev_b32_e32 v19, 3, v201
	v_xor_b32_e32 v19, v19, v201
	v_and_b32_e32 v19, 0x100, v19
	v_xor_b32_e32 v201, v201, v19
	v_lshlrev_b32_e32 v19, 3, v19
	v_xor_b32_e32 v201, v201, v19
	v_and_b32_e32 v9, 31, v8
	v_ashrrev_i32_e32 v21, 7, v8
	s_waitcnt vmcnt(0)
	v_and_b32_e32 v8, 0x70, v8
	v_or3_b32 v18, v25, v22, v18
	v_add_u32_e32 v202, 0, v18
	v_lshrrev_b32_e32 v18, 3, v202
	v_xor_b32_e32 v18, v18, v202
	v_and_b32_e32 v18, 0x100, v18
	v_xor_b32_e32 v202, v202, v18
	v_lshlrev_b32_e32 v18, 3, v18
	v_xor_b32_e32 v202, v202, v18
	v_lshlrev_b32_e32 v33, 8, v9
	v_and_b32_e32 v42, 0x70, v26
	v_add_u32_e32 v184, s2, v21
	v_max_i32_e32 v21, 4, v184
	v_add_u32_e32 v21, -4, v21
	v_min_u32_e32 v185, 24, v21
	v_and_or_b32 v183, v27, 32, v9
	v_or_b32_e32 v34, 32, v32
	v_bitop3_b32 v34, v34, v33, v42 bitop3:0xde
	v_add_u32_e32 v200, 0, v34
	s_cmp_lg_u32 0, -1
	s_cselect_b32 s3, 0, 0
	v_add_u32_e32 v186, s3, v181
	v_add_u32_e32 v188, 7, v185
	ds_write_b128 v201, v[10:13]
	v_lshlrev_b32_e32 v10, 8, v20
	v_bitop3_b32 v10, v23, v10, v8 bitop3:0xde
	v_add_u32_e32 v203, 0, v10
	ds_write_b128 v202, v[14:17]
	ds_write_b128 v203, v[4:7] offset:32768
	v_lshlrev_b32_e32 v4, 8, v24
	v_bitop3_b32 v4, v23, v4, v8 bitop3:0xde
	v_add_u32_e32 v204, 0, v4
	ds_write_b128 v204, v[0:3] offset:32768
	v_bitop3_b32 v0, v32, v33, v42 bitop3:0xde
	v_add_u32_e32 v198, 0, v0
	s_waitcnt lgkmcnt(0)
	s_barrier
	ds_read_b128 v[0:3], v198 offset:32768
	ds_read_b128 v[4:7], v198 offset:40960
	s_waitcnt vmcnt(7) lgkmcnt(1)
	v_mfma_f32_32x32x16_bf16 v[16:31], v[0:3], v[120:123], 0
	ds_read_b128 v[34:37], v200 offset:32768
	ds_read_b128 v[38:41], v200 offset:40960
	s_waitcnt lgkmcnt(2)
	v_mfma_f32_32x32x16_bf16 v[0:15], v[4:7], v[120:123], 0
	s_waitcnt vmcnt(6) lgkmcnt(1)
	v_mfma_f32_32x32x16_bf16 v[16:31], v[34:37], v[124:127], v[16:31]
	v_or_b32_e32 v34, 64, v32
	v_bitop3_b32 v34, v34, v33, v42 bitop3:0xde
	v_add_u32_e32 v199, 0, v34
	s_waitcnt lgkmcnt(0)
	v_mfma_f32_32x32x16_bf16 v[0:15], v[38:41], v[124:127], v[0:15]
	ds_read_b128 v[34:37], v199 offset:32768
	ds_read_b128 v[38:41], v199 offset:40960
	s_waitcnt vmcnt(5) lgkmcnt(1)
	v_mfma_f32_32x32x16_bf16 v[16:31], v[34:37], v[116:119], v[16:31]
	v_or_b32_e32 v34, 0x60, v32
	v_bitop3_b32 v34, v34, v33, v42 bitop3:0xde
	v_add_u32_e32 v193, 0, v34
	s_waitcnt lgkmcnt(0)
	v_mfma_f32_32x32x16_bf16 v[0:15], v[38:41], v[116:119], v[0:15]
	ds_read_b128 v[34:37], v193 offset:32768
	ds_read_b128 v[38:41], v193 offset:40960
	s_waitcnt vmcnt(4) lgkmcnt(1)
	v_mfma_f32_32x32x16_bf16 v[16:31], v[34:37], v[112:115], v[16:31]
	v_or_b32_e32 v34, 0x80, v32
	v_bitop3_b32 v34, v34, v33, v42 bitop3:0xde
	v_add_u32_e32 v192, 0, v34
	s_waitcnt lgkmcnt(0)
	v_mfma_f32_32x32x16_bf16 v[0:15], v[38:41], v[112:115], v[0:15]
	ds_read_b128 v[34:37], v192 offset:32768
	ds_read_b128 v[38:41], v192 offset:40960
	s_waitcnt vmcnt(3) lgkmcnt(1)
	v_mfma_f32_32x32x16_bf16 v[16:31], v[34:37], v[108:111], v[16:31]
	v_or_b32_e32 v34, 0xa0, v32
	v_bitop3_b32 v34, v34, v33, v42 bitop3:0xde
	v_add_u32_e32 v191, 0, v34
	s_waitcnt lgkmcnt(0)
	v_mfma_f32_32x32x16_bf16 v[0:15], v[38:41], v[108:111], v[0:15]
	ds_read_b128 v[34:37], v191 offset:32768
	ds_read_b128 v[38:41], v191 offset:40960
	s_waitcnt vmcnt(2) lgkmcnt(1)
	v_mfma_f32_32x32x16_bf16 v[16:31], v[34:37], v[104:107], v[16:31]
	v_or_b32_e32 v34, 0xc0, v32
	v_bitop3_b32 v34, v34, v33, v42 bitop3:0xde
	v_add_u32_e32 v190, 0, v34
	v_or_b32_e32 v32, 0xe0, v32
	v_bitop3_b32 v32, v32, v33, v42 bitop3:0xde
	v_add_u32_e32 v189, 0, v32
	s_waitcnt lgkmcnt(0)
	v_mfma_f32_32x32x16_bf16 v[0:15], v[38:41], v[104:107], v[0:15]
	ds_read_b128 v[34:37], v190 offset:32768
	ds_read_b128 v[38:41], v190 offset:40960
	s_waitcnt vmcnt(1) lgkmcnt(1)
	v_mfma_f32_32x32x16_bf16 v[16:31], v[34:37], v[100:103], v[16:31]
	s_waitcnt lgkmcnt(0)
	v_mfma_f32_32x32x16_bf16 v[0:15], v[38:41], v[100:103], v[0:15]
	ds_read_b128 v[32:35], v189 offset:32768
	ds_read_b128 v[36:39], v189 offset:40960
	s_waitcnt vmcnt(0) lgkmcnt(1)
	v_mfma_f32_32x32x16_bf16 v[16:31], v[32:35], v[96:99], v[16:31]
	s_waitcnt lgkmcnt(0)
	v_mfma_f32_32x32x16_bf16 v[0:15], v[36:39], v[96:99], v[0:15]
	s_nop 9
	v_max_f32_e32 v32, v17, v17
	v_max_f32_e32 v33, v16, v16
	v_max_f32_e32 v32, v33, v32
	v_max_f32_e32 v33, v25, v25
	v_max_f32_e32 v34, v24, v24
	v_max_f32_e32 v33, v34, v33
	v_max3_f32 v32, v32, v18, v19
	v_max_f32_e32 v34, v9, v9
	v_max_f32_e32 v35, v8, v8
	v_max_f32_e32 v34, v35, v34
	v_max3_f32 v35, v0, v1, v2
	v_max3_f32 v34, v34, v10, v11
	v_max3_f32 v33, v33, v26, v27
	v_max3_f32 v35, v35, v3, v4
	v_max3_f32 v34, v34, v12, v13
	v_max3_f32 v32, v32, v20, v21
	v_max3_f32 v33, v33, v28, v29
	v_max3_f32 v35, v35, v5, v6
	v_max3_f32 v34, v34, v14, v15
	v_max3_f32 v32, v32, v22, v23
	v_max3_f32 v33, v33, v30, v31
	v_max3_f32 v34, v35, v7, v34
	v_max3_f32 v32, v32, v33, v34
	v_mov_b32_e32 v33, v32
	s_nop 1
	v_permlane32_swap_b32_e32 v32, v33
	v_max_f32_e32 v33, v33, v33
	v_max_f32_e32 v32, v32, v32
	v_max_f32_e32 v32, v32, v33
	v_add_f32_e32 v33, 0x7149f2ca, v32
	v_max_f32_e32 v32, 0xf149f2ca, v32
	v_cmp_ge_f32_e32 vcc, s31, v33
	v_sub_f32_e32 v33, 0xf149f2ca, v32
	v_mul_f32_e32 v33, 0x3e0293ee, v33
	s_cmp_eq_u64 vcc, exec
	v_exp_f32_e32 v33, v33
	s_cselect_b64 vcc, -1, 0
	v_cndmask_b32_e32 v206, v32, v230, vcc
	s_add_u32 s2, s8, s76
	v_mul_f32_e32 v32, 0xbe0293ee, v206
	s_addc_u32 s3, s9, s77
	v_cndmask_b32_e64 v205, v33, 1.0, vcc
	v_mov_b32_e32 v33, v32
	s_add_u32 s10, s6, s76
	v_fmac_f32_e32 v33, 0x3e0293ee, v31
	s_addc_u32 s11, s7, s77
	v_pk_fma_f32 v[146:147], v[14:15], s[52:53], v[32:33] op_sel_hi:[1,0,0]
	v_pk_fma_f32 v[148:149], v[12:13], s[52:53], v[32:33] op_sel_hi:[1,0,0]
	v_pk_fma_f32 v[150:151], v[10:11], s[52:53], v[32:33] op_sel_hi:[1,0,0]
	v_pk_fma_f32 v[152:153], v[8:9], s[52:53], v[32:33] op_sel_hi:[1,0,0]
	v_pk_fma_f32 v[154:155], v[6:7], s[52:53], v[32:33] op_sel_hi:[1,0,0]
	v_pk_fma_f32 v[156:157], v[4:5], s[52:53], v[32:33] op_sel_hi:[1,0,0]
	v_pk_fma_f32 v[158:159], v[2:3], s[52:53], v[32:33] op_sel_hi:[1,0,0]
	v_pk_fma_f32 v[160:161], v[0:1], s[52:53], v[32:33] op_sel_hi:[1,0,0]
	global_load_dwordx4 v[0:3], v128, s[2:3]
	global_load_dwordx4 v[4:7], v178, s[2:3]
	global_load_dwordx4 v[8:11], v128, s[10:11]
	global_load_dwordx4 v[12:15], v178, s[10:11]
	s_add_u32 s2, s2, s76
	s_addc_u32 s3, s3, s77
	s_add_u32 s10, s10, s76
	s_addc_u32 s11, s11, s77
	global_load_dwordx4 v[130:133], v128, s[2:3]
	global_load_dwordx4 v[134:137], v178, s[2:3]
	global_load_dwordx4 v[138:141], v128, s[10:11]
	global_load_dwordx4 v[142:145], v178, s[10:11]
	v_fmamk_f32 v16, v16, 0x3e0293ee, v32
	v_fmamk_f32 v17, v17, 0x3e0293ee, v32
	v_fmamk_f32 v18, v18, 0x3e0293ee, v32
	v_fmamk_f32 v19, v19, 0x3e0293ee, v32
	v_fmamk_f32 v20, v20, 0x3e0293ee, v32
	v_fmamk_f32 v21, v21, 0x3e0293ee, v32
	v_fmamk_f32 v22, v22, 0x3e0293ee, v32
	v_fmamk_f32 v23, v23, 0x3e0293ee, v32
	v_fmamk_f32 v24, v24, 0x3e0293ee, v32
	v_fmamk_f32 v25, v25, 0x3e0293ee, v32
	v_fmamk_f32 v26, v26, 0x3e0293ee, v32
	v_fmamk_f32 v27, v27, 0x3e0293ee, v32
	v_fmamk_f32 v28, v28, 0x3e0293ee, v32
	v_fmamk_f32 v29, v29, 0x3e0293ee, v32
	v_fmamk_f32 v30, v30, 0x3e0293ee, v32
	v_exp_f32_e32 v176, v16
	v_exp_f32_e32 v211, v17
	v_exp_f32_e32 v163, v18
	v_exp_f32_e32 v177, v19
	v_exp_f32_e32 v164, v20
	v_exp_f32_e32 v175, v21
	v_exp_f32_e32 v165, v22
	v_exp_f32_e32 v174, v23
	v_exp_f32_e32 v166, v24
	v_exp_f32_e32 v173, v25
	v_exp_f32_e32 v167, v26
	v_exp_f32_e32 v172, v27
	v_exp_f32_e32 v168, v28
	v_exp_f32_e32 v171, v29
	v_exp_f32_e32 v169, v30
	v_exp_f32_e32 v170, v33
	s_waitcnt vmcnt(4)
	ds_write_b128 v201, v[0:3] offset:16384
	ds_write_b128 v202, v[4:7] offset:16384
	ds_write_b128 v203, v[8:11] offset:49152
	ds_write_b128 v204, v[12:15] offset:49152
	v_mov_b32_e32 v15, 0
	s_cmp_lt_i32 s19, 3
	s_waitcnt lgkmcnt(0)
	s_barrier
	s_cbranch_scc1 .LBB0_838
	s_add_i32 s20, s17, -4
	s_add_i32 s21, s19, -1
	s_cmp_lg_u32 0, -1
	s_cselect_b32 s2, 0, 0
	s_addk_i32 s2, 0x4000
	s_movk_i32 s3, 0x7c
	v_add_u32_e32 v207, s2, v181
	s_mul_i32 s2, s17, 0x7c
	v_mul_lo_u32 v0, v184, s3
	v_sub_u32_e32 v0, s2, v0
	s_add_i32 s2, 0, 0x14a2c
	v_mov_b32_e32 v187, 0
	v_mov_b32_e32 v179, v129
	v_add_u32_e32 v208, s2, v0
	s_mov_b32 s23, 4
	s_movk_i32 s22, 0xc0
	v_mov_b32_e32 v48, 0
	v_mov_b32_e32 v49, v187
	v_mov_b32_e32 v50, v187
	v_mov_b32_e32 v51, v187
	v_mov_b32_e32 v52, v187
	v_mov_b32_e32 v53, v187
	v_mov_b32_e32 v54, v187
	v_mov_b32_e32 v55, v187
	v_mov_b32_e32 v56, v187
	v_mov_b32_e32 v57, v187
	v_mov_b32_e32 v58, v187
	v_mov_b32_e32 v59, v187
	v_mov_b32_e32 v60, v187
	v_mov_b32_e32 v61, v187
	v_mov_b32_e32 v62, v187
	v_mov_b32_e32 v63, v187
	v_mov_b32_e32 v32, 0
	v_mov_b32_e32 v33, v187
	v_mov_b32_e32 v34, v187
	v_mov_b32_e32 v35, v187
	v_mov_b32_e32 v36, v187
	v_mov_b32_e32 v37, v187
	v_mov_b32_e32 v38, v187
	v_mov_b32_e32 v39, v187
	v_mov_b32_e32 v40, v187
	v_mov_b32_e32 v41, v187
	v_mov_b32_e32 v42, v187
	v_mov_b32_e32 v43, v187
	v_mov_b32_e32 v44, v187
	v_mov_b32_e32 v45, v187
	v_mov_b32_e32 v46, v187
	v_mov_b32_e32 v47, v187
	v_mov_b32_e32 v16, 0
	v_mov_b32_e32 v17, v187
	v_mov_b32_e32 v18, v187
	v_mov_b32_e32 v19, v187
	v_mov_b32_e32 v20, v187
	v_mov_b32_e32 v21, v187
	v_mov_b32_e32 v22, v187
	v_mov_b32_e32 v23, v187
	v_mov_b32_e32 v24, v187
	v_mov_b32_e32 v25, v187
	v_mov_b32_e32 v26, v187
	v_mov_b32_e32 v27, v187
	v_mov_b32_e32 v28, v187
	v_mov_b32_e32 v29, v187
	v_mov_b32_e32 v30, v187
	v_mov_b32_e32 v31, v187
	v_mov_b32_e32 v0, 0
	v_mov_b32_e32 v1, v187
	v_mov_b32_e32 v2, v187
	v_mov_b32_e32 v3, v187
	v_mov_b32_e32 v4, v187
	v_mov_b32_e32 v5, v187
	v_mov_b32_e32 v6, v187
	v_mov_b32_e32 v7, v187
	v_mov_b32_e32 v8, v187
	v_mov_b32_e32 v9, v187
	v_mov_b32_e32 v10, v187
	v_mov_b32_e32 v11, v187
	v_mov_b32_e32 v12, v187
	v_mov_b32_e32 v13, v187
	v_mov_b32_e32 v14, v187
	v_mov_b32_e32 v15, v187
	.p2alignl 6, 3212836864

.LBB0_860:
	s_waitcnt vmcnt(4)
	v_add_u32_e32 v41, 32, v72
	v_and_b32_e32 v36, 63, v71
	v_and_b32_e32 v37, 0xfffff0, v72
	v_lshlrev_b32_e32 v38, 1, v72
	v_and_b32_e32 v42, 0xfffff0, v41
	v_lshlrev_b32_e32 v43, 1, v41
	v_and_or_b32 v37, v38, 8, v37
	v_and_or_b32 v42, v43, 8, v42
	v_lshlrev_b32_e32 v44, 4, v36
	s_and_b64 s[2:3], s[22:23], exec
	v_lshrrev_b32_e32 v38, 1, v72
	v_lshrrev_b32_e32 v37, 1, v37
	v_lshrrev_b32_e32 v39, 5, v74
	v_and_b32_e32 v40, 3, v72
	v_lshrrev_b32_e32 v42, 1, v42
	v_lshlrev_b32_e32 v43, 3, v36
	v_and_b32_e32 v45, 0xc0, v44
	v_lshlrev_b32_e32 v36, 1, v36
	s_cselect_b32 s22, 4, 36
	v_or_b32_e32 v37, v37, v39
	v_and_or_b32 v38, v38, 4, v40
	v_lshlrev_b32_e32 v40, 1, v74
	v_or_b32_e32 v39, v42, v39
	v_and_or_b32 v45, v43, 24, v45
	v_and_b32_e32 v36, 32, v36
	v_and_b32_e32 v43, 0x100, v43
	s_cmp_lg_u32 0, -1
	v_lshlrev_b32_e32 v37, 9, v37
	v_lshlrev_b32_e32 v38, 6, v38
	v_lshlrev_b32_e32 v39, 9, v39
	v_or3_b32 v48, v45, v36, v43
	v_and_b32_e32 v36, 48, v40
	s_cselect_b32 s24, 0, 0
	s_add_i32 s2, 0, 0x15000
	v_or3_b32 v37, v37, v38, v36
	v_or3_b32 v36, v39, v38, v36
	v_lshl_add_u32 v38, v73, 12, s2
	v_add_u32_e32 v204, v38, v44
	s_waitcnt vmcnt(3)
	ds_write_b128 v204, v[24:27]
	s_waitcnt vmcnt(2)
	ds_write_b128 v204, v[20:23] offset:1024
	s_waitcnt vmcnt(1)
	ds_write_b128 v204, v[32:35] offset:2048
	s_waitcnt vmcnt(0)
	ds_write_b128 v204, v[28:31] offset:3072
	v_add_u32_e32 v205, 0, v37
	v_lshrrev_b32_e32 v37, 3, v205
	v_xor_b32_e32 v37, v37, v205
	v_and_b32_e32 v37, 0x100, v37
	v_xor_b32_e32 v205, v205, v37
	v_lshlrev_b32_e32 v37, 3, v37
	v_xor_b32_e32 v205, v205, v37
	ds_write_b128 v205, v[12:15]
	v_lshlrev_b32_e32 v12, 8, v72
	v_and_b32_e32 v13, 0x70, v71
	v_bitop3_b32 v12, v40, v12, v13 bitop3:0xde
	v_add_u32_e32 v206, 0, v36
	v_lshrrev_b32_e32 v36, 3, v206
	v_xor_b32_e32 v36, v36, v206
	v_and_b32_e32 v36, 0x100, v36
	v_xor_b32_e32 v206, v206, v36
	v_lshlrev_b32_e32 v36, 3, v36
	v_xor_b32_e32 v206, v206, v36
	v_add_u32_e32 v207, 0, v12
	ds_write_b128 v206, v[16:19]
	ds_write_b128 v207, v[8:11] offset:32768
	v_lshlrev_b32_e32 v8, 8, v41
	v_bitop3_b32 v8, v40, v8, v13 bitop3:0xde
	v_add_u32_e32 v208, 0, v8
	v_and_b32_e32 v42, 0xffffff80, v96
	ds_write_b128 v208, v[4:7] offset:32768
	v_xor_b32_e32 v4, v96, v71
	s_movk_i32 s2, 0x70
	v_and_or_b32 v49, v4, s2, v42
	s_add_i32 s2, 0, 0x10000
	v_add_u32_e32 v4, s2, v49
	ds_write_b128 v4, v[0:3]
	v_lshlrev_b32_e32 v0, 4, v70
	v_lshlrev_b32_e32 v58, 8, v70
	v_and_b32_e32 v59, 0x70, v0
	v_bitop3_b32 v0, v68, v58, v59 bitop3:0xde
	v_add_u32_e32 v209, 0, v0
	s_waitcnt lgkmcnt(0)
	s_barrier
	ds_read_b128 v[16:19], v209 offset:32768
	ds_read_b128 v[20:23], v209 offset:40960
	s_waitcnt lgkmcnt(1)
	v_mfma_f32_32x32x16_bf16 v[32:47], v[16:19], v[158:161], 0
	v_or_b32_e32 v62, 32, v68
	v_bitop3_b32 v50, v62, v58, v59 bitop3:0xde
	v_add_u32_e32 v211, 0, v50
	ds_read_b128 v[50:53], v211 offset:32768
	ds_read_b128 v[54:57], v211 offset:40960
	v_or_b32_e32 v63, 64, v68
	v_or_b32_e32 v64, 0x60, v68
	v_lshlrev_b32_e32 v65, 7, v70
	s_waitcnt lgkmcnt(2)
	v_mfma_f32_32x32x16_bf16 v[16:31], v[20:23], v[158:161], 0
	s_mov_b32 s72, s73
	s_mov_b32 s74, s73
	s_mov_b32 s75, s73
	s_mov_b32 s76, s73
	s_mov_b32 s77, s73
	s_mov_b32 s78, s73
	s_mov_b32 s79, s73
	s_waitcnt lgkmcnt(1)
	v_mfma_f32_32x32x16_bf16 v[32:47], v[50:53], v[154:157], v[32:47]
	v_bitop3_b32 v50, v63, v58, v59 bitop3:0xde
	v_add_u32_e32 v212, 0, v50
	s_mov_b32 s80, s73
	s_mov_b32 s81, s73
	s_mov_b32 s82, s73
	s_mov_b32 s83, s73
	s_mov_b32 s84, s73
	s_waitcnt lgkmcnt(0)
	v_mfma_f32_32x32x16_bf16 v[16:31], v[54:57], v[154:157], v[16:31]
	ds_read_b128 v[50:53], v212 offset:32768
	ds_read_b128 v[54:57], v212 offset:40960
	s_mov_b32 s85, s73
	s_mov_b32 s86, s73
	s_mov_b32 s87, s73
	v_mov_b64_e32 v[0:1], s[72:73]
	v_mov_b32_e32 v183, v129
	v_mov_b32_e32 v97, v129
	s_waitcnt lgkmcnt(1)
	v_mfma_f32_32x32x16_bf16 v[32:47], v[50:53], v[150:153], v[32:47]
	v_bitop3_b32 v50, v64, v58, v59 bitop3:0xde
	v_add_u32_e32 v213, 0, v50
	v_mov_b64_e32 v[2:3], s[74:75]
	v_mov_b64_e32 v[4:5], s[76:77]
	v_mov_b64_e32 v[6:7], s[78:79]
	v_mov_b64_e32 v[8:9], s[80:81]
	v_mov_b64_e32 v[10:11], s[82:83]
	s_waitcnt lgkmcnt(0)
	v_mfma_f32_32x32x16_bf16 v[16:31], v[54:57], v[150:153], v[16:31]
	ds_read_b128 v[50:53], v213 offset:32768
	ds_read_b128 v[54:57], v213 offset:40960
	v_mov_b64_e32 v[12:13], s[84:85]
	v_mov_b64_e32 v[14:15], s[86:87]
	v_add_u32_e32 v228, 0, v49
	v_add_u32_e32 v201, s24, v48
	v_add_u32_e32 v229, 0x12000, v228
	s_waitcnt lgkmcnt(1)
	v_mfma_f32_32x32x16_bf16 v[32:47], v[50:53], v[146:149], v[32:47]
	v_or_b32_e32 v50, 0x80, v68
	v_bitop3_b32 v50, v50, v58, v59 bitop3:0xde
	v_add_u32_e32 v215, 0, v50
	v_lshl_add_u64 v[184:185], s[58:59], 0, v[96:97]
	v_lshl_add_u64 v[186:187], s[8:9], 0, v[96:97]
	v_mov_b32_e32 v210, 0
	v_readlane_b32 s80, v255, 48
	s_waitcnt lgkmcnt(0)
	v_mfma_f32_32x32x16_bf16 v[16:31], v[54:57], v[146:149], v[16:31]
	ds_read_b128 v[50:53], v215 offset:32768
	ds_read_b128 v[54:57], v215 offset:40960
	s_movk_i32 s84, 0xffe0
	s_waitcnt lgkmcnt(1)
	v_mfma_f32_32x32x16_bf16 v[32:47], v[50:53], v[142:145], v[32:47]
	v_or_b32_e32 v50, 0xa0, v68
	v_bitop3_b32 v50, v50, v58, v59 bitop3:0xde
	v_add_u32_e32 v217, 0, v50
	s_waitcnt lgkmcnt(0)
	v_mfma_f32_32x32x16_bf16 v[16:31], v[54:57], v[142:145], v[16:31]
	ds_read_b128 v[50:53], v217 offset:32768
	ds_read_b128 v[54:57], v217 offset:40960
	s_waitcnt lgkmcnt(1)
	v_mfma_f32_32x32x16_bf16 v[32:47], v[50:53], v[138:141], v[32:47]
	v_or_b32_e32 v50, 0xc0, v68
	v_bitop3_b32 v50, v50, v58, v59 bitop3:0xde
	v_add_u32_e32 v214, 0, v50
	s_waitcnt lgkmcnt(0)
	v_mfma_f32_32x32x16_bf16 v[16:31], v[54:57], v[138:141], v[16:31]
	ds_read_b128 v[50:53], v214 offset:32768
	ds_read_b128 v[54:57], v214 offset:40960
	s_waitcnt lgkmcnt(1)
	v_mfma_f32_32x32x16_bf16 v[32:47], v[50:53], v[134:137], v[32:47]
	v_or_b32_e32 v50, 0xe0, v68
	v_bitop3_b32 v50, v50, v58, v59 bitop3:0xde
	v_add_u32_e32 v216, 0, v50
	s_waitcnt lgkmcnt(0)
	v_mfma_f32_32x32x16_bf16 v[16:31], v[54:57], v[134:137], v[16:31]
	ds_read_b128 v[50:53], v216 offset:32768
	ds_read_b128 v[54:57], v216 offset:40960
	s_waitcnt lgkmcnt(1)
	v_mfma_f32_32x32x16_bf16 v[32:47], v[50:53], v[130:133], v[32:47]
	v_lshlrev_b32_e32 v50, 3, v70
	v_and_b32_e32 v66, 0x70, v50
	v_bitop3_b32 v218, v68, v65, v66 bitop3:0xde
	v_add_u32_e32 v219, s2, v218
	v_bitop3_b32 v220, v62, v65, v66 bitop3:0xde
	v_add_u32_e32 v221, s2, v220
	v_bitop3_b32 v222, v63, v65, v66 bitop3:0xde
	s_waitcnt lgkmcnt(0)
	v_mfma_f32_32x32x16_bf16 v[16:31], v[54:57], v[130:133], v[16:31]
	ds_read_b128 v[50:53], v219
	ds_read_b128 v[54:57], v219 offset:4096
	ds_read_b128 v[58:61], v204
	v_add_u32_e32 v223, s2, v222
	v_bitop3_b32 v224, v64, v65, v66 bitop3:0xde
	v_add_u32_e32 v225, s2, v224
	s_waitcnt lgkmcnt(0)
	v_mfma_f32_32x32x16_bf16 v[32:47], v[50:53], v[58:61], v[32:47]
	v_mfma_f32_32x32x16_bf16 v[16:31], v[54:57], v[58:61], v[16:31]
	ds_read_b128 v[50:53], v221
	ds_read_b128 v[54:57], v221 offset:4096
	ds_read_b128 v[58:61], v204 offset:1024
	s_waitcnt lgkmcnt(0)
	v_mfma_f32_32x32x16_bf16 v[32:47], v[50:53], v[58:61], v[32:47]
	v_mfma_f32_32x32x16_bf16 v[16:31], v[54:57], v[58:61], v[16:31]
	ds_read_b128 v[50:53], v223
	ds_read_b128 v[54:57], v223 offset:4096
	ds_read_b128 v[58:61], v204 offset:2048
	s_waitcnt lgkmcnt(0)
	v_mfma_f32_32x32x16_bf16 v[32:47], v[50:53], v[58:61], v[32:47]
	v_mfma_f32_32x32x16_bf16 v[16:31], v[54:57], v[58:61], v[16:31]
	ds_read_b128 v[50:53], v225
	ds_read_b128 v[54:57], v225 offset:4096
	ds_read_b128 v[58:61], v204 offset:3072
	s_waitcnt lgkmcnt(0)
	v_mfma_f32_32x32x16_bf16 v[32:47], v[50:53], v[58:61], v[32:47]
	v_mfma_f32_32x32x16_bf16 v[16:31], v[54:57], v[58:61], v[16:31]
	s_nop 10
	v_max_f32_e32 v50, v33, v33
	v_max_f32_e32 v51, v32, v32
	v_max_f32_e32 v50, v51, v50
	v_max_f32_e32 v51, v41, v41
	v_max_f32_e32 v52, v40, v40
	v_max_f32_e32 v51, v52, v51
	v_max3_f32 v50, v50, v34, v35
	v_max_f32_e32 v52, v25, v25
	v_max_f32_e32 v53, v24, v24
	v_max_f32_e32 v52, v53, v52
	v_max3_f32 v53, v16, v17, v18
	v_max3_f32 v52, v52, v26, v27
	v_max3_f32 v51, v51, v42, v43
	v_max3_f32 v53, v53, v19, v20
	v_max3_f32 v52, v52, v28, v29
	v_max3_f32 v50, v50, v36, v37
	v_max3_f32 v51, v51, v44, v45
	v_max3_f32 v53, v53, v21, v22
	v_max3_f32 v52, v52, v30, v31
	v_max3_f32 v50, v50, v38, v39
	v_max3_f32 v51, v51, v46, v47
	v_max3_f32 v52, v53, v23, v52
	v_max3_f32 v50, v50, v51, v52
	v_mov_b32_e32 v51, v50
	s_nop 1
	v_permlane32_swap_b32_e32 v50, v51
	v_max_f32_e32 v51, v51, v51
	v_max_f32_e32 v50, v50, v50
	v_max_f32_e32 v50, v50, v51
	v_add_f32_e32 v51, 0x7149f2ca, v50
	v_max_f32_e32 v50, 0xf149f2ca, v50
	v_cmp_ge_f32_e32 vcc, s34, v51
	v_sub_f32_e32 v51, 0xf149f2ca, v50
	v_mul_f32_e32 v51, 0x3dd53b94, v51
	s_cmp_eq_u64 vcc, exec
	v_exp_f32_e32 v51, v51
	s_cselect_b64 vcc, -1, 0
	v_cndmask_b32_e32 v227, v50, v230, vcc
	v_mul_f32_e32 v50, 0xbdd53b94, v227
	v_cndmask_b32_e64 v226, v51, 1.0, vcc
	v_mov_b32_e32 v51, v50
	s_add_u32 s2, s18, s92
	v_fmac_f32_e32 v51, 0x3dd53b94, v47
	s_addc_u32 s3, s19, s93
	v_fmamk_f32 v32, v32, 0x3dd53b94, v50
	v_fmamk_f32 v33, v33, 0x3dd53b94, v50
	v_pk_fma_f32 v[80:81], v[16:17], s[54:55], v[50:51] op_sel_hi:[1,0,0]
	s_add_u32 s74, s16, s92
	v_lshl_add_u64 v[16:17], s[2:3], 0, v[128:129]
	v_fmamk_f32 v34, v34, 0x3dd53b94, v50
	v_fmamk_f32 v35, v35, 0x3dd53b94, v50
	v_pk_fma_f32 v[84:85], v[20:21], s[54:55], v[50:51] op_sel_hi:[1,0,0]
	v_pk_fma_f32 v[82:83], v[18:19], s[54:55], v[50:51] op_sel_hi:[1,0,0]
	v_exp_f32_e32 v64, v32
	v_exp_f32_e32 v65, v33
	s_addc_u32 s75, s17, s93
	global_load_dwordx4 v[16:19], v[16:17], off
	v_lshl_add_u64 v[20:21], s[2:3], 0, v[182:183]
	v_lshl_add_u64 v[32:33], s[96:97], 0, v[96:97]
	v_pk_fma_f32 v[88:89], v[24:25], s[54:55], v[50:51] op_sel_hi:[1,0,0]
	v_pk_fma_f32 v[86:87], v[22:23], s[54:55], v[50:51] op_sel_hi:[1,0,0]
	v_exp_f32_e32 v66, v34
	v_exp_f32_e32 v67, v35
	global_load_dwordx4 v[20:23], v[20:21], off
	v_lshl_add_u64 v[24:25], s[74:75], 0, v[128:129]
	global_load_dwordx4 v[32:35], v[32:33], off
	v_pk_fma_f32 v[92:93], v[28:29], s[54:55], v[50:51] op_sel_hi:[1,0,0]
	v_pk_fma_f32 v[90:91], v[26:27], s[54:55], v[50:51] op_sel_hi:[1,0,0]
	global_load_dwordx4 v[24:27], v[24:25], off
	v_lshl_add_u64 v[28:29], s[74:75], 0, v[182:183]
	v_pk_fma_f32 v[94:95], v[30:31], s[54:55], v[50:51] op_sel_hi:[1,0,0]
	global_load_dwordx4 v[28:31], v[28:29], off
	v_fmamk_f32 v36, v36, 0x3dd53b94, v50
	v_fmamk_f32 v37, v37, 0x3dd53b94, v50
	v_fmamk_f32 v38, v38, 0x3dd53b94, v50
	v_fmamk_f32 v39, v39, 0x3dd53b94, v50
	v_fmamk_f32 v40, v40, 0x3dd53b94, v50
	v_fmamk_f32 v41, v41, 0x3dd53b94, v50
	v_fmamk_f32 v42, v42, 0x3dd53b94, v50
	v_fmamk_f32 v43, v43, 0x3dd53b94, v50
	v_fmamk_f32 v44, v44, 0x3dd53b94, v50
	v_fmamk_f32 v45, v45, 0x3dd53b94, v50
	v_fmamk_f32 v46, v46, 0x3dd53b94, v50
	v_exp_f32_e32 v68, v36
	v_exp_f32_e32 v69, v37
	v_exp_f32_e32 v70, v38
	v_exp_f32_e32 v71, v39
	v_exp_f32_e32 v72, v40
	v_exp_f32_e32 v73, v41
	v_exp_f32_e32 v74, v42
	v_exp_f32_e32 v75, v43
	v_exp_f32_e32 v76, v44
	v_exp_f32_e32 v77, v45
	v_exp_f32_e32 v78, v46
	v_exp_f32_e32 v79, v51
	s_waitcnt vmcnt(0)
	ds_write_b128 v205, v[16:19] offset:16384
	ds_write_b128 v206, v[20:23] offset:16384
	ds_write_b128 v207, v[24:27] offset:49152
	ds_write_b128 v208, v[28:31] offset:49152
	s_addk_i32 s24, 0x4000
	v_lshl_add_u64 v[16:17], s[20:21], 0, v[128:129]
	v_lshl_add_u64 v[18:19], s[20:21], 0, v[182:183]
	ds_write_b128 v229, v[32:35]
	v_add_u32_e32 v203, s24, v48
	v_lshl_add_u64 v[188:189], s[12:13], 0, v[16:17]
	v_lshl_add_u64 v[190:191], s[12:13], 0, v[18:19]
	v_lshl_add_u64 v[192:193], s[14:15], 0, v[16:17]
	v_lshl_add_u64 v[198:199], s[14:15], 0, v[18:19]
	v_mov_b64_e32 v[62:63], v[14:15]
	v_mov_b64_e32 v[46:47], v[14:15]
	v_mov_b64_e32 v[30:31], v[14:15]
	s_add_i32 s23, s22, -1
	s_mov_b32 s20, 2
	v_mov_b64_e32 v[60:61], v[12:13]
	v_mov_b64_e32 v[58:59], v[10:11]
	v_mov_b64_e32 v[56:57], v[8:9]
	v_mov_b64_e32 v[54:55], v[6:7]
	v_mov_b64_e32 v[52:53], v[4:5]
	v_mov_b64_e32 v[50:51], v[2:3]
	v_mov_b64_e32 v[48:49], v[0:1]
	v_mov_b64_e32 v[44:45], v[12:13]
	v_mov_b64_e32 v[42:43], v[10:11]
	v_mov_b64_e32 v[40:41], v[8:9]
	v_mov_b64_e32 v[38:39], v[6:7]
	v_mov_b64_e32 v[36:37], v[4:5]
	v_mov_b64_e32 v[34:35], v[2:3]
	v_mov_b64_e32 v[32:33], v[0:1]
	v_mov_b64_e32 v[28:29], v[12:13]
	v_mov_b64_e32 v[26:27], v[10:11]
	v_mov_b64_e32 v[24:25], v[8:9]
	v_mov_b64_e32 v[22:23], v[6:7]
	v_mov_b64_e32 v[20:21], v[4:5]
	v_mov_b64_e32 v[18:19], v[2:3]
	v_mov_b64_e32 v[16:17], v[0:1]
	v_readlane_b32 s21, v252, 17
	s_waitcnt lgkmcnt(0)
	s_barrier
	.p2alignl 6, 3212836864

.LBB0_880:
	v_add_u32_e32 v21, 32, v185
	v_and_b32_e32 v17, 0xfffff0, v185
	v_lshlrev_b32_e32 v18, 1, v185
	v_and_b32_e32 v22, 0xfffff0, v21
	v_lshlrev_b32_e32 v23, 1, v21
	v_and_b32_e32 v16, 63, v184
	v_and_or_b32 v17, v18, 8, v17
	v_and_or_b32 v22, v23, 8, v22
	v_lshrrev_b32_e32 v17, 1, v17
	v_lshrrev_b32_e32 v19, 5, v186
	v_lshrrev_b32_e32 v22, 1, v22
	v_lshlrev_b32_e32 v23, 4, v16
	v_lshrrev_b32_e32 v18, 1, v185
	v_or_b32_e32 v17, v17, v19
	v_and_b32_e32 v20, 3, v185
	v_or_b32_e32 v19, v22, v19
	v_lshlrev_b32_e32 v22, 3, v16
	v_and_b32_e32 v23, 0xc0, v23
	v_lshlrev_b32_e32 v16, 1, v16
	v_and_or_b32 v18, v18, 4, v20
	v_lshlrev_b32_e32 v20, 1, v186
	v_and_or_b32 v23, v22, 24, v23
	v_and_b32_e32 v16, 32, v16
	v_and_b32_e32 v22, 0x100, v22
	v_lshlrev_b32_e32 v17, 9, v17
	v_lshlrev_b32_e32 v18, 6, v18
	v_or3_b32 v114, v23, v16, v22
	v_and_b32_e32 v16, 48, v20
	v_or3_b32 v17, v17, v18, v16
	v_add_u32_e32 v212, 0, v17
	v_lshrrev_b32_e32 v17, 3, v212
	v_xor_b32_e32 v17, v17, v212
	v_and_b32_e32 v17, 0x100, v17
	v_xor_b32_e32 v212, v212, v17
	v_lshlrev_b32_e32 v17, 3, v17
	v_xor_b32_e32 v212, v212, v17
	v_lshlrev_b32_e32 v19, 9, v19
	v_cvt_pk_bf16_f32 v138, v176, v177
	v_cvt_pk_bf16_f32 v139, v170, v171
	v_cvt_pk_bf16_f32 v140, v164, v165
	v_cvt_pk_bf16_f32 v141, v144, v145
	v_cvt_pk_bf16_f32 v154, v142, v143
	v_cvt_pk_bf16_f32 v155, v136, v137
	v_cvt_pk_bf16_f32 v156, v134, v135
	v_cvt_pk_bf16_f32 v157, v132, v133
	v_cvt_pk_bf16_f32 v158, v130, v131
	v_cvt_pk_bf16_f32 v159, v126, v127
	v_cvt_pk_bf16_f32 v160, v124, v125
	v_cvt_pk_bf16_f32 v161, v122, v123
	v_cvt_pk_bf16_f32 v150, v120, v121
	v_cvt_pk_bf16_f32 v151, v118, v119
	v_cvt_pk_bf16_f32 v152, v116, v117
	v_cvt_pk_bf16_f32 v153, v112, v113
	v_cvt_pk_bf16_f32 v146, v108, v109
	v_cvt_pk_bf16_f32 v147, v110, v111
	v_cvt_pk_bf16_f32 v148, v104, v105
	v_cvt_pk_bf16_f32 v149, v106, v107
	v_cvt_pk_bf16_f32 v142, v100, v101
	v_cvt_pk_bf16_f32 v143, v102, v103
	v_cvt_pk_bf16_f32 v144, v96, v97
	v_cvt_pk_bf16_f32 v145, v98, v99
	v_cvt_pk_bf16_f32 v134, v92, v93
	v_cvt_pk_bf16_f32 v135, v94, v95
	v_cvt_pk_bf16_f32 v136, v88, v89
	v_cvt_pk_bf16_f32 v137, v90, v91
	v_cvt_pk_bf16_f32 v130, v84, v85
	v_cvt_pk_bf16_f32 v131, v86, v87
	v_cvt_pk_bf16_f32 v132, v80, v81
	v_cvt_pk_bf16_f32 v133, v82, v83
	s_waitcnt vmcnt(0)
	ds_write_b128 v212, v[8:11]
	v_lshlrev_b32_e32 v8, 8, v185
	v_and_b32_e32 v9, 0x70, v184
	v_or3_b32 v16, v19, v18, v16
	v_bitop3_b32 v8, v20, v8, v9 bitop3:0xde
	v_add_u32_e32 v213, 0, v16
	v_lshrrev_b32_e32 v16, 3, v213
	v_xor_b32_e32 v16, v16, v213
	v_and_b32_e32 v16, 0x100, v16
	v_xor_b32_e32 v213, v213, v16
	v_lshlrev_b32_e32 v16, 3, v16
	v_xor_b32_e32 v213, v213, v16
	v_add_u32_e32 v214, 0, v8
	ds_write_b128 v213, v[12:15]
	ds_write_b128 v214, v[4:7] offset:32768
	v_lshlrev_b32_e32 v4, 8, v21
	v_bitop3_b32 v4, v20, v4, v9 bitop3:0xde
	v_add_u32_e32 v215, 0, v4
	ds_write_b128 v215, v[0:3] offset:32768
	v_lshlrev_b32_e32 v0, 4, v163
	v_lshlrev_b32_e32 v56, 8, v163
	v_and_b32_e32 v57, 0x70, v0
	v_bitop3_b32 v0, v162, v56, v57 bitop3:0xde
	v_add_u32_e32 v216, 0, v0
	s_waitcnt lgkmcnt(0)
	s_barrier
	s_add_u32 s16, s10, s96
	s_addc_u32 s17, s11, s97
	s_add_u32 s18, s8, s96
	s_addc_u32 s19, s9, s97
	global_load_dwordx4 v[178:181], v128, s[16:17]
	global_load_dwordx4 v[182:185], v198, s[16:17]
	global_load_dwordx4 v[186:189], v128, s[18:19]
	global_load_dwordx4 v[190:193], v198, s[18:19]
	ds_read_b128 v[16:19], v216 offset:32768
	ds_read_b128 v[20:23], v216 offset:40960
	s_waitcnt lgkmcnt(1)
	v_mfma_f32_32x32x16_bf16 v[32:47], v[16:19], v[138:141], 0
	v_or_b32_e32 v48, 32, v162
	v_bitop3_b32 v48, v48, v56, v57 bitop3:0xde
	v_add_u32_e32 v218, 0, v48
	ds_read_b128 v[48:51], v218 offset:32768
	ds_read_b128 v[52:55], v218 offset:40960
	s_cmp_lg_u32 0, -1
	s_cselect_b32 s53, 0, 0
	s_add_u32 s16, s10, s96
	s_waitcnt lgkmcnt(2)
	v_mfma_f32_32x32x16_bf16 v[16:31], v[20:23], v[138:141], 0
	s_addc_u32 s17, s11, s97
	v_mov_b32_e32 v199, v129
	s_add_u32 s18, s8, s96
	s_addc_u32 s19, s9, s97
	s_add_u32 s2, s16, s96
	s_addc_u32 s3, s17, s97
	s_waitcnt lgkmcnt(1)
	v_mfma_f32_32x32x16_bf16 v[32:47], v[48:51], v[154:157], v[32:47]
	v_or_b32_e32 v48, 64, v162
	v_bitop3_b32 v48, v48, v56, v57 bitop3:0xde
	v_add_u32_e32 v219, 0, v48
	v_lshl_add_u64 v[64:65], s[2:3], 0, v[128:129]
	s_mov_b32 s72, s73
	s_mov_b32 s74, s73
	s_mov_b32 s75, s73
	s_waitcnt lgkmcnt(0)
	v_mfma_f32_32x32x16_bf16 v[16:31], v[52:55], v[154:157], v[16:31]
	ds_read_b128 v[48:51], v219 offset:32768
	ds_read_b128 v[52:55], v219 offset:40960
	s_mov_b32 s76, s73
	s_mov_b32 s77, s73
	s_mov_b32 s78, s73
	s_mov_b32 s79, s73
	s_mov_b32 s80, s73
	s_mov_b32 s81, s73
	s_waitcnt lgkmcnt(1)
	v_mfma_f32_32x32x16_bf16 v[32:47], v[48:51], v[158:161], v[32:47]
	v_or_b32_e32 v48, 0x60, v162
	v_bitop3_b32 v48, v48, v56, v57 bitop3:0xde
	v_add_u32_e32 v220, 0, v48
	s_mov_b32 s82, s73
	s_mov_b32 s83, s73
	s_mov_b32 s84, s73
	s_mov_b32 s85, s73
	s_waitcnt lgkmcnt(0)
	v_mfma_f32_32x32x16_bf16 v[16:31], v[52:55], v[158:161], v[16:31]
	ds_read_b128 v[48:51], v220 offset:32768
	ds_read_b128 v[52:55], v220 offset:40960
	s_mov_b32 s86, s73
	s_mov_b32 s87, s73
	v_mov_b64_e32 v[0:1], s[72:73]
	v_mov_b64_e32 v[14:15], s[86:87]
	v_add_u32_e32 v209, s53, v114
	v_mov_b64_e32 v[2:3], s[74:75]
	s_waitcnt lgkmcnt(1)
	v_mfma_f32_32x32x16_bf16 v[32:47], v[48:51], v[150:153], v[32:47]
	v_or_b32_e32 v48, 0x80, v162
	v_bitop3_b32 v48, v48, v56, v57 bitop3:0xde
	v_add_u32_e32 v221, 0, v48
	v_mov_b64_e32 v[4:5], s[76:77]
	v_mov_b64_e32 v[6:7], s[78:79]
	v_mov_b64_e32 v[8:9], s[80:81]
	v_mov_b64_e32 v[10:11], s[82:83]
	s_waitcnt lgkmcnt(0)
	v_mfma_f32_32x32x16_bf16 v[16:31], v[52:55], v[150:153], v[16:31]
	ds_read_b128 v[48:51], v221 offset:32768
	ds_read_b128 v[52:55], v221 offset:40960
	v_mov_b64_e32 v[12:13], s[84:85]
	s_mov_b32 s39, 4
	v_mov_b32_e32 v217, 0
	v_readlane_b32 s80, v255, 48
	s_movk_i32 s79, 0xff
	s_movk_i32 s84, 0xffe0
	s_waitcnt lgkmcnt(1)
	v_mfma_f32_32x32x16_bf16 v[32:47], v[48:51], v[146:149], v[32:47]
	v_or_b32_e32 v48, 0xa0, v162
	v_bitop3_b32 v48, v48, v56, v57 bitop3:0xde
	v_add_u32_e32 v222, 0, v48
	s_waitcnt lgkmcnt(0)
	v_mfma_f32_32x32x16_bf16 v[16:31], v[52:55], v[146:149], v[16:31]
	ds_read_b128 v[48:51], v222 offset:32768
	ds_read_b128 v[52:55], v222 offset:40960
	s_waitcnt lgkmcnt(1)
	v_mfma_f32_32x32x16_bf16 v[32:47], v[48:51], v[142:145], v[32:47]
	v_or_b32_e32 v48, 0xc0, v162
	v_bitop3_b32 v48, v48, v56, v57 bitop3:0xde
	v_add_u32_e32 v224, 0, v48
	s_waitcnt lgkmcnt(0)
	v_mfma_f32_32x32x16_bf16 v[16:31], v[52:55], v[142:145], v[16:31]
	ds_read_b128 v[48:51], v224 offset:32768
	ds_read_b128 v[52:55], v224 offset:40960
	s_waitcnt lgkmcnt(1)
	v_mfma_f32_32x32x16_bf16 v[32:47], v[48:51], v[134:137], v[32:47]
	v_or_b32_e32 v48, 0xe0, v162
	v_bitop3_b32 v48, v48, v56, v57 bitop3:0xde
	v_add_u32_e32 v223, 0, v48
	s_waitcnt lgkmcnt(0)
	v_mfma_f32_32x32x16_bf16 v[16:31], v[52:55], v[134:137], v[16:31]
	ds_read_b128 v[48:51], v223 offset:32768
	ds_read_b128 v[52:55], v223 offset:40960
	global_load_dwordx4 v[162:165], v[64:65], off
	v_lshl_add_u64 v[64:65], s[2:3], 0, v[198:199]
	s_waitcnt lgkmcnt(1)
	v_mfma_f32_32x32x16_bf16 v[32:47], v[48:51], v[130:133], v[32:47]
	global_load_dwordx4 v[166:169], v[64:65], off
	s_waitcnt lgkmcnt(0)
	v_mfma_f32_32x32x16_bf16 v[16:31], v[52:55], v[130:133], v[16:31]
	s_nop 8
	s_add_u32 s16, s18, s96
	s_addc_u32 s17, s19, s97
	v_lshl_add_u64 v[64:65], s[16:17], 0, v[128:129]
	global_load_dwordx4 v[170:173], v[64:65], off
	v_lshl_add_u64 v[64:65], s[16:17], 0, v[198:199]
	global_load_dwordx4 v[174:177], v[64:65], off
	s_and_b64 s[2:3], s[14:15], exec
	s_cselect_b32 s14, 3, 35
	v_exp_f32_e32 v64, v32
	v_exp_f32_e32 v65, v33
	v_exp_f32_e32 v66, v34
	v_exp_f32_e32 v67, v35
	v_exp_f32_e32 v68, v36
	v_exp_f32_e32 v69, v37
	v_exp_f32_e32 v70, v38
	v_exp_f32_e32 v71, v39
	v_exp_f32_e32 v72, v40
	v_exp_f32_e32 v73, v41
	v_exp_f32_e32 v74, v42
	v_exp_f32_e32 v80, v16
	v_exp_f32_e32 v81, v17
	v_exp_f32_e32 v75, v43
	v_exp_f32_e32 v76, v44
	v_exp_f32_e32 v77, v45
	v_exp_f32_e32 v78, v46
	v_exp_f32_e32 v79, v47
	v_exp_f32_e32 v82, v18
	v_exp_f32_e32 v83, v19
	v_lshl_add_u64 v[16:17], s[12:13], 0, v[128:129]
	v_lshl_add_u64 v[18:19], s[12:13], 0, v[198:199]
	v_exp_f32_e32 v94, v30
	v_exp_f32_e32 v95, v31
	v_exp_f32_e32 v92, v28
	v_exp_f32_e32 v93, v29
	v_exp_f32_e32 v196, v26
	v_exp_f32_e32 v197, v27
	v_exp_f32_e32 v194, v24
	v_exp_f32_e32 v195, v25
	v_exp_f32_e32 v86, v22
	v_exp_f32_e32 v87, v23
	v_exp_f32_e32 v84, v20
	v_exp_f32_e32 v85, v21
	s_addk_i32 s53, 0x4000
	v_lshl_add_u64 v[200:201], s[64:65], 0, v[16:17]
	v_lshl_add_u64 v[202:203], s[64:65], 0, v[18:19]
	v_lshl_add_u64 v[204:205], s[66:67], 0, v[16:17]
	v_lshl_add_u64 v[206:207], s[66:67], 0, v[18:19]
	v_mov_b64_e32 v[62:63], v[14:15]
	v_mov_b64_e32 v[46:47], v[14:15]
	v_mov_b64_e32 v[30:31], v[14:15]
	v_add_u32_e32 v211, s53, v114
	v_mov_b64_e32 v[60:61], v[12:13]
	v_mov_b64_e32 v[58:59], v[10:11]
	v_mov_b64_e32 v[56:57], v[8:9]
	v_mov_b64_e32 v[54:55], v[6:7]
	v_mov_b64_e32 v[52:53], v[4:5]
	v_mov_b64_e32 v[50:51], v[2:3]
	v_mov_b64_e32 v[48:49], v[0:1]
	v_mov_b64_e32 v[44:45], v[12:13]
	v_mov_b64_e32 v[42:43], v[10:11]
	v_mov_b64_e32 v[40:41], v[8:9]
	v_mov_b64_e32 v[38:39], v[6:7]
	v_mov_b64_e32 v[36:37], v[4:5]
	v_mov_b64_e32 v[34:35], v[2:3]
	v_mov_b64_e32 v[32:33], v[0:1]
	v_mov_b64_e32 v[28:29], v[12:13]
	v_mov_b64_e32 v[26:27], v[10:11]
	v_mov_b64_e32 v[24:25], v[8:9]
	v_mov_b64_e32 v[22:23], v[6:7]
	v_mov_b64_e32 v[20:21], v[4:5]
	v_mov_b64_e32 v[18:19], v[2:3]
	v_mov_b64_e32 v[16:17], v[0:1]
	s_waitcnt vmcnt(4)
	ds_write_b128 v212, v[178:181] offset:16384
	ds_write_b128 v213, v[182:185] offset:16384
	ds_write_b128 v214, v[186:189] offset:49152
	ds_write_b128 v215, v[190:193] offset:49152
	s_mov_b32 s53, 0x38e38e39
	s_waitcnt lgkmcnt(0)
	s_barrier
	.p2alignl 6, 3212836864

.LBB0_967:
	s_and_b64 s[2:3], s[86:87], exec
	s_cselect_b32 s2, s79, s38
	s_lshr_b32 s2, s2, 12
	s_and_b32 s72, s2, 0x80000
	s_and_b64 s[2:3], s[86:87], exec
	s_cselect_b32 s15, s83, s19
	s_cselect_b32 s17, s82, s18
	s_cselect_b32 s67, s23, s85
	s_cselect_b32 s3, s22, s84
	s_cmp_lt_i32 s38, 0
	s_cselect_b64 s[96:97], -1, 0
	s_add_u32 s24, s18, 0x80
	s_addc_u32 s25, s19, 0
	v_lshl_add_u64 v[0:1], s[24:25], 0, v[202:203]
	v_lshl_add_u64 v[206:207], v[0:1], 0, s[20:21]
	v_lshl_add_u64 v[0:1], s[24:25], 0, v[204:205]
	v_mov_b32_e32 v128, v129
	v_lshl_add_u64 v[208:209], v[0:1], 0, s[20:21]
	s_add_u32 s2, s84, 0x100
	s_waitcnt vmcnt(0)
	v_mov_b32_e32 v130, v129
	v_mov_b32_e32 v131, v129
	v_mov_b32_e32 v64, 0
	v_mov_b64_e32 v[0:1], v[128:129]
	v_mov_b64_e32 v[4:5], v[128:129]
	v_mov_b64_e32 v[16:17], v[128:129]
	v_mov_b64_e32 v[20:21], v[128:129]
	v_mov_b64_e32 v[32:33], v[128:129]
	v_mov_b64_e32 v[36:37], v[128:129]
	v_mov_b64_e32 v[48:49], v[128:129]
	v_mov_b64_e32 v[52:53], v[128:129]
	v_mov_b64_e32 v[8:9], v[128:129]
	v_mov_b64_e32 v[12:13], v[128:129]
	v_mov_b64_e32 v[24:25], v[128:129]
	v_mov_b64_e32 v[28:29], v[128:129]
	v_mov_b64_e32 v[40:41], v[128:129]
	v_mov_b64_e32 v[44:45], v[128:129]
	v_mov_b64_e32 v[56:57], v[128:129]
	v_mov_b64_e32 v[60:61], v[128:129]
	s_addc_u32 s29, s85, 0
	s_mov_b32 s30, -2
	v_mov_b64_e32 v[2:3], v[130:131]
	v_mov_b64_e32 v[6:7], v[130:131]
	v_mov_b64_e32 v[18:19], v[130:131]
	v_mov_b64_e32 v[22:23], v[130:131]
	v_mov_b64_e32 v[34:35], v[130:131]
	v_mov_b64_e32 v[38:39], v[130:131]
	v_mov_b64_e32 v[50:51], v[130:131]
	v_mov_b64_e32 v[54:55], v[130:131]
	v_mov_b64_e32 v[10:11], v[130:131]
	v_mov_b64_e32 v[14:15], v[130:131]
	v_mov_b64_e32 v[26:27], v[130:131]
	v_mov_b64_e32 v[30:31], v[130:131]
	v_mov_b64_e32 v[42:43], v[130:131]
	v_mov_b64_e32 v[46:47], v[130:131]
	v_mov_b64_e32 v[58:59], v[130:131]
	v_mov_b64_e32 v[62:63], v[130:131]
	v_mov_b32_e32 v65, v64
	v_mov_b32_e32 v66, v64
	v_mov_b32_e32 v67, v64
	v_mov_b32_e32 v68, v64
	v_mov_b32_e32 v69, v64
	v_mov_b32_e32 v70, v64
	v_mov_b32_e32 v71, v64
	v_mov_b32_e32 v80, v64
	v_mov_b32_e32 v81, v64
	v_mov_b32_e32 v82, v64
	v_mov_b32_e32 v83, v64
	v_mov_b32_e32 v84, v64
	v_mov_b32_e32 v85, v64
	v_mov_b32_e32 v86, v64
	v_mov_b32_e32 v87, v64
	v_mov_b32_e32 v96, v64
	v_mov_b32_e32 v97, v64
	v_mov_b32_e32 v98, v64
	v_mov_b32_e32 v99, v64
	v_mov_b32_e32 v100, v64
	v_mov_b32_e32 v101, v64
	v_mov_b32_e32 v102, v64
	v_mov_b32_e32 v103, v64
	v_mov_b32_e32 v124, v64
	v_mov_b32_e32 v125, v64
	v_mov_b32_e32 v126, v64
	v_mov_b32_e32 v127, v64
	v_mov_b32_e32 v134, v64
	v_mov_b32_e32 v135, v64
	v_mov_b32_e32 v136, v64
	v_mov_b32_e32 v137, v64
	v_mov_b32_e32 v72, v64
	v_mov_b32_e32 v73, v64
	v_mov_b32_e32 v74, v64
	v_mov_b32_e32 v75, v64
	v_mov_b32_e32 v76, v64
	v_mov_b32_e32 v77, v64
	v_mov_b32_e32 v78, v64
	v_mov_b32_e32 v79, v64
	v_mov_b32_e32 v88, v64
	v_mov_b32_e32 v89, v64
	v_mov_b32_e32 v90, v64
	v_mov_b32_e32 v91, v64
	v_mov_b32_e32 v92, v64
	v_mov_b32_e32 v93, v64
	v_mov_b32_e32 v94, v64
	v_mov_b32_e32 v95, v64
	v_mov_b32_e32 v112, v64
	v_mov_b32_e32 v113, v64
	v_mov_b32_e32 v114, v64
	v_mov_b32_e32 v115, v64
	v_mov_b32_e32 v120, v64
	v_mov_b32_e32 v121, v64
	v_mov_b32_e32 v122, v64
	v_mov_b32_e32 v123, v64
	v_mov_b32_e32 v138, v64
	v_mov_b32_e32 v139, v64
	v_mov_b32_e32 v140, v64
	v_mov_b32_e32 v141, v64
	v_mov_b32_e32 v142, v64
	v_mov_b32_e32 v143, v64
	v_mov_b32_e32 v144, v64
	v_mov_b32_e32 v145, v64
	s_branch .LBB0_969
	.p2alignl 6, 3212836864

.LBB0_1398:
	v_mov_b32_e32 v128, v129
	s_cmp_lt_i32 s25, 0
	v_mov_b32_e32 v213, v129
	v_mov_b32_e32 v215, v129
	v_lshl_add_u64 v[220:221], v[2:3], 0, s[46:47]
	v_mov_b32_e32 v130, v129
	v_mov_b32_e32 v131, v129
	v_mov_b32_e32 v64, 0
	v_mov_b64_e32 v[0:1], v[128:129]
	v_mov_b64_e32 v[4:5], v[128:129]
	v_mov_b64_e32 v[16:17], v[128:129]
	v_mov_b64_e32 v[20:21], v[128:129]
	v_mov_b64_e32 v[32:33], v[128:129]
	v_mov_b64_e32 v[36:37], v[128:129]
	v_mov_b64_e32 v[48:49], v[128:129]
	v_mov_b64_e32 v[52:53], v[128:129]
	v_mov_b64_e32 v[8:9], v[128:129]
	v_mov_b64_e32 v[12:13], v[128:129]
	v_mov_b64_e32 v[24:25], v[128:129]
	v_mov_b64_e32 v[28:29], v[128:129]
	v_mov_b64_e32 v[40:41], v[128:129]
	v_mov_b64_e32 v[44:45], v[128:129]
	v_mov_b64_e32 v[56:57], v[128:129]
	v_mov_b64_e32 v[60:61], v[128:129]
	s_cselect_b64 s[20:21], -1, 0
	v_lshl_add_u64 v[216:217], s[14:15], 0, v[214:215]
	v_lshl_add_u64 v[218:219], s[14:15], 0, v[212:213]
	s_mov_b32 s24, -2
	s_mov_b64 s[74:75], 0
	v_mov_b64_e32 v[2:3], v[130:131]
	v_mov_b64_e32 v[6:7], v[130:131]
	v_mov_b64_e32 v[18:19], v[130:131]
	v_mov_b64_e32 v[22:23], v[130:131]
	v_mov_b64_e32 v[34:35], v[130:131]
	v_mov_b64_e32 v[38:39], v[130:131]
	v_mov_b64_e32 v[50:51], v[130:131]
	v_mov_b64_e32 v[54:55], v[130:131]
	v_mov_b64_e32 v[10:11], v[130:131]
	v_mov_b64_e32 v[14:15], v[130:131]
	v_mov_b64_e32 v[26:27], v[130:131]
	v_mov_b64_e32 v[30:31], v[130:131]
	v_mov_b64_e32 v[42:43], v[130:131]
	v_mov_b64_e32 v[46:47], v[130:131]
	v_mov_b64_e32 v[58:59], v[130:131]
	v_mov_b64_e32 v[62:63], v[130:131]
	v_mov_b32_e32 v65, v64
	v_mov_b32_e32 v66, v64
	v_mov_b32_e32 v67, v64
	v_mov_b32_e32 v68, v64
	v_mov_b32_e32 v69, v64
	v_mov_b32_e32 v70, v64
	v_mov_b32_e32 v71, v64
	v_mov_b32_e32 v80, v64
	v_mov_b32_e32 v81, v64
	v_mov_b32_e32 v82, v64
	v_mov_b32_e32 v83, v64
	v_mov_b32_e32 v84, v64
	v_mov_b32_e32 v85, v64
	v_mov_b32_e32 v86, v64
	v_mov_b32_e32 v87, v64
	v_mov_b32_e32 v96, v64
	v_mov_b32_e32 v97, v64
	v_mov_b32_e32 v98, v64
	v_mov_b32_e32 v99, v64
	v_mov_b32_e32 v100, v64
	v_mov_b32_e32 v101, v64
	v_mov_b32_e32 v102, v64
	v_mov_b32_e32 v103, v64
	v_mov_b32_e32 v112, v64
	v_mov_b32_e32 v113, v64
	v_mov_b32_e32 v114, v64
	v_mov_b32_e32 v115, v64
	v_mov_b32_e32 v116, v64
	v_mov_b32_e32 v117, v64
	v_mov_b32_e32 v118, v64
	v_mov_b32_e32 v119, v64
	v_mov_b32_e32 v72, v64
	v_mov_b32_e32 v73, v64
	v_mov_b32_e32 v74, v64
	v_mov_b32_e32 v75, v64
	v_mov_b32_e32 v76, v64
	v_mov_b32_e32 v77, v64
	v_mov_b32_e32 v78, v64
	v_mov_b32_e32 v79, v64
	v_mov_b32_e32 v88, v64
	v_mov_b32_e32 v89, v64
	v_mov_b32_e32 v90, v64
	v_mov_b32_e32 v91, v64
	v_mov_b32_e32 v92, v64
	v_mov_b32_e32 v93, v64
	v_mov_b32_e32 v94, v64
	v_mov_b32_e32 v95, v64
	v_mov_b32_e32 v104, v64
	v_mov_b32_e32 v105, v64
	v_mov_b32_e32 v106, v64
	v_mov_b32_e32 v107, v64
	v_mov_b32_e32 v108, v64
	v_mov_b32_e32 v109, v64
	v_mov_b32_e32 v110, v64
	v_mov_b32_e32 v111, v64
	v_mov_b32_e32 v120, v64
	v_mov_b32_e32 v121, v64
	v_mov_b32_e32 v122, v64
	v_mov_b32_e32 v123, v64
	v_mov_b32_e32 v124, v64
	v_mov_b32_e32 v125, v64
	v_mov_b32_e32 v126, v64
	v_mov_b32_e32 v127, v64
	s_branch .LBB0_1400
	.p2alignl 6, 3212836864

.LBB0_1441:
	s_lshl_b32 s2, s18, 3
	s_ashr_i32 s3, s2, 31
	s_lshl_b64 s[2:3], s[2:3], 2
	s_add_u32 s20, s27, s2
	v_mov_b32_e32 v0, 0
	s_addc_u32 s21, s28, s3
	s_mov_b32 s19, 0
	v_mov_b32_e32 v1, v0
	v_mov_b32_e32 v2, v0
	v_mov_b32_e32 v3, v0
	v_mov_b32_e32 v4, v0
	v_mov_b32_e32 v5, v0
	v_mov_b32_e32 v6, v0
	v_mov_b32_e32 v7, v0
	v_mov_b32_e32 v12, v0
	v_mov_b32_e32 v13, v0
	v_mov_b32_e32 v14, v0
	v_mov_b32_e32 v15, v0
	v_mov_b32_e32 v20, v0
	v_mov_b32_e32 v21, v0
	v_mov_b32_e32 v22, v0
	v_mov_b32_e32 v23, v0
	v_mov_b32_e32 v28, v0
	v_mov_b32_e32 v29, v0
	v_mov_b32_e32 v30, v0
	v_mov_b32_e32 v31, v0
	v_mov_b32_e32 v36, v0
	v_mov_b32_e32 v37, v0
	v_mov_b32_e32 v38, v0
	v_mov_b32_e32 v39, v0
	v_mov_b32_e32 v44, v0
	v_mov_b32_e32 v45, v0
	v_mov_b32_e32 v46, v0
	v_mov_b32_e32 v47, v0
	v_mov_b32_e32 v52, v0
	v_mov_b32_e32 v53, v0
	v_mov_b32_e32 v54, v0
	v_mov_b32_e32 v55, v0
	v_mov_b32_e32 v8, v0
	v_mov_b32_e32 v9, v0
	v_mov_b32_e32 v10, v0
	v_mov_b32_e32 v11, v0
	v_mov_b32_e32 v16, v0
	v_mov_b32_e32 v17, v0
	v_mov_b32_e32 v18, v0
	v_mov_b32_e32 v19, v0
	v_mov_b32_e32 v24, v0
	v_mov_b32_e32 v25, v0
	v_mov_b32_e32 v26, v0
	v_mov_b32_e32 v27, v0
	v_mov_b32_e32 v32, v0
	v_mov_b32_e32 v33, v0
	v_mov_b32_e32 v34, v0
	v_mov_b32_e32 v35, v0
	v_mov_b32_e32 v40, v0
	v_mov_b32_e32 v41, v0
	v_mov_b32_e32 v42, v0
	v_mov_b32_e32 v43, v0
	v_mov_b32_e32 v48, v0
	v_mov_b32_e32 v49, v0
	v_mov_b32_e32 v50, v0
	v_mov_b32_e32 v51, v0
	v_mov_b32_e32 v56, v0
	v_mov_b32_e32 v57, v0
	v_mov_b32_e32 v58, v0
	v_mov_b32_e32 v59, v0
	v_mov_b32_e32 v60, v0
	v_mov_b32_e32 v61, v0
	v_mov_b32_e32 v62, v0
	v_mov_b32_e32 v63, v0
	v_mov_b32_e32 v64, v0
	v_mov_b32_e32 v65, v0
	v_mov_b32_e32 v66, v0
	v_mov_b32_e32 v67, v0
	v_mov_b32_e32 v68, v0
	v_mov_b32_e32 v69, v0
	v_mov_b32_e32 v70, v0
	v_mov_b32_e32 v71, v0
	v_mov_b32_e32 v76, v0
	v_mov_b32_e32 v77, v0
	v_mov_b32_e32 v78, v0
	v_mov_b32_e32 v79, v0
	v_mov_b32_e32 v84, v0
	v_mov_b32_e32 v85, v0
	v_mov_b32_e32 v86, v0
	v_mov_b32_e32 v87, v0
	v_mov_b32_e32 v92, v0
	v_mov_b32_e32 v93, v0
	v_mov_b32_e32 v94, v0
	v_mov_b32_e32 v95, v0
	v_mov_b32_e32 v100, v0
	v_mov_b32_e32 v101, v0
	v_mov_b32_e32 v102, v0
	v_mov_b32_e32 v103, v0
	v_mov_b32_e32 v108, v0
	v_mov_b32_e32 v109, v0
	v_mov_b32_e32 v110, v0
	v_mov_b32_e32 v111, v0
	v_mov_b32_e32 v116, v0
	v_mov_b32_e32 v117, v0
	v_mov_b32_e32 v118, v0
	v_mov_b32_e32 v119, v0
	v_mov_b32_e32 v72, v0
	v_mov_b32_e32 v73, v0
	v_mov_b32_e32 v74, v0
	v_mov_b32_e32 v75, v0
	v_mov_b32_e32 v80, v0
	v_mov_b32_e32 v81, v0
	v_mov_b32_e32 v82, v0
	v_mov_b32_e32 v83, v0
	v_mov_b32_e32 v88, v0
	v_mov_b32_e32 v89, v0
	v_mov_b32_e32 v90, v0
	v_mov_b32_e32 v91, v0
	v_mov_b32_e32 v96, v0
	v_mov_b32_e32 v97, v0
	v_mov_b32_e32 v98, v0
	v_mov_b32_e32 v99, v0
	v_mov_b32_e32 v104, v0
	v_mov_b32_e32 v105, v0
	v_mov_b32_e32 v106, v0
	v_mov_b32_e32 v107, v0
	v_mov_b32_e32 v112, v0
	v_mov_b32_e32 v113, v0
	v_mov_b32_e32 v114, v0
	v_mov_b32_e32 v115, v0
	v_mov_b32_e32 v120, v0
	v_mov_b32_e32 v121, v0
	v_mov_b32_e32 v122, v0
	v_mov_b32_e32 v123, v0
	v_mov_b32_e32 v124, v0
	v_mov_b32_e32 v125, v0
	v_mov_b32_e32 v126, v0
	v_mov_b32_e32 v127, v0
	s_branch .LBB0_1444
	.p2alignl 6, 3212836864
